# second dead d_ws region (S5 scratch) holds the first 85 score slots of every workgroup: nearly all groups of the largest blocks use stored scores
# speedup vs baseline: 1.0474x; 1.0014x over previous
.LBB0_1297:
	v_readlane_b32 s14, v254, 48
	v_readlane_b32 s15, v254, 49
	s_andn2_b64 vcc, exec, s[14:15]
	s_cbranch_vccnz .LBB0_1558
	s_waitcnt lgkmcnt(0)
	s_add_u32 s22, s20, 0x2c200000
	s_addc_u32 s23, s21, 0
	s_add_u32 s18, s20, 0x3f700000
	s_addc_u32 s19, s21, 0
	s_add_u32 s24, s20, 0x2c400000
	s_addc_u32 s25, s21, 0
	s_add_u32 s26, s20, 0x2b200000
	v_readlane_b32 s14, v255, 0
	s_addc_u32 s27, s21, 0
	s_mov_b32 s76, s14
	s_lshr_b32 s32, s14, 1
	s_sub_i32 s100, 488, s32
	s_add_i32 s101, s32, -1
	s_mul_i32 s101, s101, s32
	s_bitcmp1_b32 s14, 0
	s_cselect_b32 s32, s32, 0
	s_add_i32 s101, s101, s32
	s_mul_i32 s32, s14, 404
	s_sub_i32 s101, s32, s101
	s_add_i32 s101, s101, -85
	s_mul_i32 s101, s101, 0x600
	s_add_u32 s101, s101, 0x35d00000
	v_mbcnt_lo_u32_b32 v230, -1, 0
	v_mbcnt_hi_u32_b32 v230, -1, v230
	v_lshlrev_b32_e32 v197, 3, v230
	v_lshlrev_b32_e32 v230, 4, v230
	v_add_u32_e32 v230, s101, v230
	v_add_u32_e32 v197, s101, v197
	v_add_u32_e32 v197, 0x400, v197
	s_mul_i32 s32, s14, 130560
	s_add_u32 s32, s32, 0x2dd00000
	s_sub_u32 s101, s32, s101
	v_readlane_b32 s15, v255, 1
	s_branch .LBB0_1300

.LBB0_1308:
	s_waitcnt vmcnt(5)
	v_mfma_f32_16x16x32_bf16 v[130:133], v[116:119], v[0:3], 0
	v_mfma_f32_16x16x32_bf16 v[156:159], v[116:119], v[244:247], 0
	s_min_i32 s32, s15, s100
	s_cmp_lt_i32 s32, 85
	s_cselect_b32 vcc_lo, s101, 0
	s_mul_i32 s32, s32, 0x600
	s_add_i32 s32, s32, vcc_lo
	v_add_u32_e32 v231, s32, v230
	v_add_u32_e32 v222, s32, v197
	s_add_i32 s31, s15, 8
	s_min_i32 s35, s31, s14
	v_lshl_or_b32 v72, s35, 5, v125
	s_waitcnt vmcnt(3)
	v_mfma_f32_16x16x32_bf16 v[134:137], v[112:115], v[0:3], 0
	v_mfma_f32_16x16x32_bf16 v[160:163], v[112:115], v[244:247], 0
	v_ashrrev_i32_e32 v73, 31, v72
	v_lshlrev_b64 v[72:73], 7, v[72:73]
	v_sub_u32_e32 v72, v72, v229
	v_lshl_add_u64 v[84:85], v[120:121], 0, v[72:73]
	v_mfma_f32_16x16x32_bf16 v[138:141], v[108:111], v[4:7], v[130:133]
	v_mfma_f32_16x16x32_bf16 v[156:159], v[108:111], v[248:251], v[156:159]
	global_load_dwordx4 v[72:75], v[84:85], off
	global_load_dwordx4 v[76:79], v[84:85], off offset:1024
	global_load_dwordx4 v[80:83], v[84:85], off offset:2048
	s_nop 0
	global_load_dwordx4 v[84:87], v[84:85], off offset:3072
	global_store_dwordx4 v232, v[216:219], s[20:21]
	global_store_dwordx2 v223, v[220:221], s[20:21]
	s_nop 1
	s_nop 0
	s_add_i32 s15, s15, 16
	s_waitcnt vmcnt(8)
	v_mfma_f32_16x16x32_bf16 v[132:135], v[104:107], v[4:7], v[134:137]
	v_mfma_f32_16x16x32_bf16 v[160:163], v[104:107], v[248:251], v[160:163]
	s_min_i32 s35, s15, s14
	s_cmp_ge_i32 s31, s82
	v_mfma_f32_16x16x32_bf16 v[142:145], v[116:119], v[16:19], 0
	v_mfma_f32_16x16x32_bf16 v[146:149], v[112:115], v[16:19], 0
	v_mfma_f32_16x16x32_bf16 v[142:145], v[108:111], v[20:23], v[142:145]
	v_mfma_f32_16x16x32_bf16 v[146:149], v[104:107], v[20:23], v[146:149]
	s_nop 3
	v_fma_f32 v156, v12, |v138|, v156
	v_fma_f32 v160, v12, |v132|, v160
	v_fma_f32 v157, v12, |v139|, v157
	v_fma_f32 v161, v12, |v133|, v161
	v_fma_f32 v158, v12, |v140|, v158
	v_fma_f32 v162, v12, |v134|, v162
	v_fma_f32 v159, v12, |v141|, v159
	v_fma_f32 v163, v12, |v135|, v163
	v_mfma_f32_16x16x32_bf16 v[138:141], v[116:119], v[24:27], 0
	v_mfma_f32_16x16x32_bf16 v[132:135], v[112:115], v[24:27], 0
	v_mfma_f32_16x16x32_bf16 v[138:141], v[108:111], v[28:31], v[138:141]
	v_mfma_f32_16x16x32_bf16 v[132:135], v[104:107], v[28:31], v[132:135]
	s_nop 3
	v_fma_f32 v156, v13, |v142|, v156
	v_fma_f32 v160, v13, |v146|, v160
	v_fma_f32 v157, v13, |v143|, v157
	v_fma_f32 v161, v13, |v147|, v161
	v_fma_f32 v158, v13, |v144|, v158
	v_fma_f32 v162, v13, |v148|, v162
	v_fma_f32 v159, v13, |v145|, v159
	v_fma_f32 v163, v13, |v149|, v163
	v_mfma_f32_16x16x32_bf16 v[142:145], v[116:119], v[32:35], 0
	v_mfma_f32_16x16x32_bf16 v[146:149], v[112:115], v[32:35], 0
	v_mfma_f32_16x16x32_bf16 v[142:145], v[108:111], v[36:39], v[142:145]
	v_mfma_f32_16x16x32_bf16 v[146:149], v[104:107], v[36:39], v[146:149]
	s_nop 3
	v_fma_f32 v156, v14, |v138|, v156
	v_fma_f32 v160, v14, |v132|, v160
	v_fma_f32 v157, v14, |v139|, v157
	v_fma_f32 v161, v14, |v133|, v161
	v_fma_f32 v158, v14, |v140|, v158
	v_fma_f32 v162, v14, |v134|, v162
	v_fma_f32 v159, v14, |v141|, v159
	v_fma_f32 v163, v14, |v135|, v163
	v_mfma_f32_16x16x32_bf16 v[138:141], v[116:119], v[40:43], 0
	v_mfma_f32_16x16x32_bf16 v[132:135], v[112:115], v[40:43], 0
	v_mfma_f32_16x16x32_bf16 v[138:141], v[108:111], v[44:47], v[138:141]
	v_mfma_f32_16x16x32_bf16 v[132:135], v[104:107], v[44:47], v[132:135]
	s_nop 3
	v_fma_f32 v156, v15, |v142|, v156
	v_fma_f32 v160, v15, |v146|, v160
	v_fma_f32 v157, v15, |v143|, v157
	v_fma_f32 v161, v15, |v147|, v161
	v_fma_f32 v158, v15, |v144|, v158
	v_fma_f32 v162, v15, |v148|, v162
	v_fma_f32 v159, v15, |v145|, v159
	v_fma_f32 v163, v15, |v149|, v163
	v_mfma_f32_16x16x32_bf16 v[142:145], v[116:119], v[48:51], 0
	v_mfma_f32_16x16x32_bf16 v[146:149], v[112:115], v[48:51], 0
	v_mfma_f32_16x16x32_bf16 v[142:145], v[108:111], v[52:55], v[142:145]
	v_mfma_f32_16x16x32_bf16 v[146:149], v[104:107], v[52:55], v[146:149]
	s_nop 3
	v_fma_f32 v156, v8, |v138|, v156
	v_fma_f32 v160, v8, |v132|, v160
	v_fma_f32 v157, v8, |v139|, v157
	v_fma_f32 v161, v8, |v133|, v161
	v_fma_f32 v158, v8, |v140|, v158
	v_fma_f32 v162, v8, |v134|, v162
	v_fma_f32 v159, v8, |v141|, v159
	v_fma_f32 v163, v8, |v135|, v163
	v_mfma_f32_16x16x32_bf16 v[138:141], v[116:119], v[56:59], 0
	v_mfma_f32_16x16x32_bf16 v[132:135], v[112:115], v[56:59], 0
	v_mfma_f32_16x16x32_bf16 v[138:141], v[108:111], v[60:63], v[138:141]
	v_mfma_f32_16x16x32_bf16 v[132:135], v[104:107], v[60:63], v[132:135]
	s_nop 3
	v_fma_f32 v156, v9, |v142|, v156
	v_fma_f32 v160, v9, |v146|, v160
	v_fma_f32 v157, v9, |v143|, v157
	v_fma_f32 v161, v9, |v147|, v161
	v_fma_f32 v158, v9, |v144|, v158
	v_fma_f32 v162, v9, |v148|, v162
	v_fma_f32 v159, v9, |v145|, v159
	v_fma_f32 v163, v9, |v149|, v163
	v_mfma_f32_16x16x32_bf16 v[142:145], v[116:119], v[64:67], 0
	v_mfma_f32_16x16x32_bf16 v[146:149], v[112:115], v[64:67], 0
	v_mfma_f32_16x16x32_bf16 v[142:145], v[108:111], v[68:71], v[142:145]
	v_mfma_f32_16x16x32_bf16 v[146:149], v[104:107], v[68:71], v[146:149]
	s_nop 3
	v_fma_f32 v156, v10, |v138|, v156
	v_fma_f32 v160, v10, |v132|, v160
	v_fma_f32 v157, v10, |v139|, v157
	v_fma_f32 v161, v10, |v133|, v161
	v_fma_f32 v158, v10, |v140|, v158
	v_fma_f32 v162, v10, |v134|, v162
	v_fma_f32 v159, v10, |v141|, v159
	v_fma_f32 v163, v10, |v135|, v163
	s_nop 7
	v_fma_f32 v156, v11, |v142|, v156
	v_fma_f32 v160, v11, |v146|, v160
	v_fma_f32 v157, v11, |v143|, v157
	v_fma_f32 v161, v11, |v147|, v161
	v_fma_f32 v158, v11, |v144|, v158
	v_fma_f32 v162, v11, |v148|, v162
	v_fma_f32 v159, v11, |v145|, v159
	v_fma_f32 v163, v11, |v149|, v163
	s_nop 0
	v_lshrrev_b32 v104, 22, v156
	v_bfe_u32 v105, v156, 21, 1
	v_lshl_add_u32 v104, v104, 2, v128
	v_mad_u32_u24 v105, v105, s1, 1
	ds_add_u32 v104, v105
	v_lshrrev_b32 v104, 22, v157
	v_bfe_u32 v105, v157, 21, 1
	v_lshl_add_u32 v104, v104, 2, v128
	v_mad_u32_u24 v105, v105, s1, 1
	ds_add_u32 v104, v105
	v_lshrrev_b32 v104, 22, v158
	v_bfe_u32 v105, v158, 21, 1
	v_lshl_add_u32 v104, v104, 2, v128
	v_mad_u32_u24 v105, v105, s1, 1
	ds_add_u32 v104, v105
	v_lshrrev_b32 v104, 22, v159
	v_bfe_u32 v105, v159, 21, 1
	v_lshl_add_u32 v104, v104, 2, v128
	v_mad_u32_u24 v105, v105, s1, 1
	ds_add_u32 v104, v105
	v_lshrrev_b32 v104, 22, v160
	v_bfe_u32 v105, v160, 21, 1
	v_lshl_add_u32 v104, v104, 2, v128
	v_mad_u32_u24 v105, v105, s1, 1
	ds_add_u32 v104, v105
	v_lshrrev_b32 v104, 22, v161
	v_bfe_u32 v105, v161, 21, 1
	v_lshl_add_u32 v104, v104, 2, v128
	v_mad_u32_u24 v105, v105, s1, 1
	ds_add_u32 v104, v105
	v_lshrrev_b32 v104, 22, v162
	v_bfe_u32 v105, v162, 21, 1
	v_lshl_add_u32 v104, v104, 2, v128
	v_mad_u32_u24 v105, v105, s1, 1
	ds_add_u32 v104, v105
	v_lshrrev_b32 v104, 22, v163
	v_bfe_u32 v105, v163, 21, 1
	v_lshl_add_u32 v104, v104, 2, v128
	v_mad_u32_u24 v105, v105, s1, 1
	ds_add_u32 v104, v105
	v_lshl_or_b32 v104, s35, 5, v125
	v_ashrrev_i32_e32 v105, 31, v104
	v_lshlrev_b64 v[104:105], 7, v[104:105]
	v_sub_u32_e32 v104, v104, v229
	v_lshl_add_u64 v[104:105], v[120:121], 0, v[104:105]
	global_load_dwordx4 v[116:119], v[104:105], off
	global_load_dwordx4 v[108:111], v[104:105], off offset:1024
	global_load_dwordx4 v[112:115], v[104:105], off offset:2048
	s_nop 0
	global_load_dwordx4 v[104:107], v[104:105], off offset:3072
	v_perm_b32 v208, v157, v156, v168
	v_perm_b32 v209, v158, v157, v169
	v_perm_b32 v210, v159, v158, v170
	v_perm_b32 v211, v161, v160, v168
	v_perm_b32 v212, v162, v161, v169
	v_perm_b32 v213, v163, v162, v170
	global_store_dwordx4 v231, v[208:211], s[20:21]
	global_store_dwordx2 v222, v[212:213], s[20:21]
	s_cbranch_scc1 .LBB0_1307
	s_waitcnt vmcnt(11)
	v_mfma_f32_16x16x32_bf16 v[130:133], v[72:75], v[0:3], 0
	v_mfma_f32_16x16x32_bf16 v[164:167], v[72:75], v[244:247], 0
	s_min_i32 s32, s31, s100
	s_cmp_lt_i32 s32, 85
	s_cselect_b32 vcc_lo, s101, 0
	s_mul_i32 s32, s32, 0x600
	s_add_i32 s32, s32, vcc_lo
	v_add_u32_e32 v232, s32, v230
	v_add_u32_e32 v223, s32, v197
	s_waitcnt vmcnt(9)
	v_mfma_f32_16x16x32_bf16 v[134:137], v[80:83], v[0:3], 0
	v_mfma_f32_16x16x32_bf16 v[186:189], v[80:83], v[244:247], 0
	v_mfma_f32_16x16x32_bf16 v[138:141], v[76:79], v[4:7], v[130:133]
	v_mfma_f32_16x16x32_bf16 v[164:167], v[76:79], v[248:251], v[164:167]
	s_waitcnt vmcnt(8)
	v_mfma_f32_16x16x32_bf16 v[132:135], v[84:87], v[4:7], v[134:137]
	v_mfma_f32_16x16x32_bf16 v[186:189], v[84:87], v[248:251], v[186:189]
	v_mfma_f32_16x16x32_bf16 v[142:145], v[72:75], v[16:19], 0
	v_mfma_f32_16x16x32_bf16 v[146:149], v[80:83], v[16:19], 0
	v_mfma_f32_16x16x32_bf16 v[142:145], v[76:79], v[20:23], v[142:145]
	v_mfma_f32_16x16x32_bf16 v[146:149], v[84:87], v[20:23], v[146:149]
	s_nop 3
	v_fma_f32 v164, v12, |v138|, v164
	v_fma_f32 v186, v12, |v132|, v186
	v_fma_f32 v165, v12, |v139|, v165
	v_fma_f32 v187, v12, |v133|, v187
	v_fma_f32 v166, v12, |v140|, v166
	v_fma_f32 v188, v12, |v134|, v188
	v_fma_f32 v167, v12, |v141|, v167
	v_fma_f32 v189, v12, |v135|, v189
	v_mfma_f32_16x16x32_bf16 v[138:141], v[72:75], v[24:27], 0
	v_mfma_f32_16x16x32_bf16 v[132:135], v[80:83], v[24:27], 0
	v_mfma_f32_16x16x32_bf16 v[138:141], v[76:79], v[28:31], v[138:141]
	v_mfma_f32_16x16x32_bf16 v[132:135], v[84:87], v[28:31], v[132:135]
	s_nop 3
	v_fma_f32 v164, v13, |v142|, v164
	v_fma_f32 v186, v13, |v146|, v186
	v_fma_f32 v165, v13, |v143|, v165
	v_fma_f32 v187, v13, |v147|, v187
	v_fma_f32 v166, v13, |v144|, v166
	v_fma_f32 v188, v13, |v148|, v188
	v_fma_f32 v167, v13, |v145|, v167
	v_fma_f32 v189, v13, |v149|, v189
	v_mfma_f32_16x16x32_bf16 v[142:145], v[72:75], v[32:35], 0
	v_mfma_f32_16x16x32_bf16 v[146:149], v[80:83], v[32:35], 0
	v_mfma_f32_16x16x32_bf16 v[142:145], v[76:79], v[36:39], v[142:145]
	v_mfma_f32_16x16x32_bf16 v[146:149], v[84:87], v[36:39], v[146:149]
	s_nop 3
	v_fma_f32 v164, v14, |v138|, v164
	v_fma_f32 v186, v14, |v132|, v186
	v_fma_f32 v165, v14, |v139|, v165
	v_fma_f32 v187, v14, |v133|, v187
	v_fma_f32 v166, v14, |v140|, v166
	v_fma_f32 v188, v14, |v134|, v188
	v_fma_f32 v167, v14, |v141|, v167
	v_fma_f32 v189, v14, |v135|, v189
	v_mfma_f32_16x16x32_bf16 v[138:141], v[72:75], v[40:43], 0
	v_mfma_f32_16x16x32_bf16 v[132:135], v[80:83], v[40:43], 0
	v_mfma_f32_16x16x32_bf16 v[138:141], v[76:79], v[44:47], v[138:141]
	v_mfma_f32_16x16x32_bf16 v[132:135], v[84:87], v[44:47], v[132:135]
	s_nop 3
	v_fma_f32 v164, v15, |v142|, v164
	v_fma_f32 v186, v15, |v146|, v186
	v_fma_f32 v165, v15, |v143|, v165
	v_fma_f32 v187, v15, |v147|, v187
	v_fma_f32 v166, v15, |v144|, v166
	v_fma_f32 v188, v15, |v148|, v188
	v_fma_f32 v167, v15, |v145|, v167
	v_fma_f32 v189, v15, |v149|, v189
	v_mfma_f32_16x16x32_bf16 v[142:145], v[72:75], v[48:51], 0
	v_mfma_f32_16x16x32_bf16 v[146:149], v[80:83], v[48:51], 0
	v_mfma_f32_16x16x32_bf16 v[142:145], v[76:79], v[52:55], v[142:145]
	v_mfma_f32_16x16x32_bf16 v[146:149], v[84:87], v[52:55], v[146:149]
	s_nop 3
	v_fma_f32 v164, v8, |v138|, v164
	v_fma_f32 v186, v8, |v132|, v186
	v_fma_f32 v165, v8, |v139|, v165
	v_fma_f32 v187, v8, |v133|, v187
	v_fma_f32 v166, v8, |v140|, v166
	v_fma_f32 v188, v8, |v134|, v188
	v_fma_f32 v167, v8, |v141|, v167
	v_fma_f32 v189, v8, |v135|, v189
	v_mfma_f32_16x16x32_bf16 v[138:141], v[72:75], v[56:59], 0
	v_mfma_f32_16x16x32_bf16 v[132:135], v[80:83], v[56:59], 0
	v_mfma_f32_16x16x32_bf16 v[138:141], v[76:79], v[60:63], v[138:141]
	v_mfma_f32_16x16x32_bf16 v[132:135], v[84:87], v[60:63], v[132:135]
	s_nop 3
	v_fma_f32 v164, v9, |v142|, v164
	v_fma_f32 v186, v9, |v146|, v186
	v_fma_f32 v165, v9, |v143|, v165
	v_fma_f32 v187, v9, |v147|, v187
	v_fma_f32 v166, v9, |v144|, v166
	v_fma_f32 v188, v9, |v148|, v188
	v_fma_f32 v167, v9, |v145|, v167
	v_fma_f32 v189, v9, |v149|, v189
	v_mfma_f32_16x16x32_bf16 v[142:145], v[72:75], v[64:67], 0
	v_mfma_f32_16x16x32_bf16 v[146:149], v[80:83], v[64:67], 0
	v_mfma_f32_16x16x32_bf16 v[142:145], v[76:79], v[68:71], v[142:145]
	v_mfma_f32_16x16x32_bf16 v[146:149], v[84:87], v[68:71], v[146:149]
	s_nop 3
	v_fma_f32 v164, v10, |v138|, v164
	v_fma_f32 v186, v10, |v132|, v186
	v_fma_f32 v165, v10, |v139|, v165
	v_fma_f32 v187, v10, |v133|, v187
	v_fma_f32 v166, v10, |v140|, v166
	v_fma_f32 v188, v10, |v134|, v188
	v_fma_f32 v167, v10, |v141|, v167
	v_fma_f32 v189, v10, |v135|, v189
	s_nop 7
	v_fma_f32 v164, v11, |v142|, v164
	v_fma_f32 v186, v11, |v146|, v186
	v_fma_f32 v165, v11, |v143|, v165
	v_fma_f32 v187, v11, |v147|, v187
	v_fma_f32 v166, v11, |v144|, v166
	v_fma_f32 v188, v11, |v148|, v188
	v_fma_f32 v167, v11, |v145|, v167
	v_fma_f32 v189, v11, |v149|, v189
	v_lshrrev_b32 v135, 22, v164
	v_bfe_u32 v131, v164, 21, 1
	v_mad_u32_u24 v131, v131, s1, 1
	v_lshl_add_u32 v135, v135, 2, v128
	ds_add_u32 v135, v131
	v_lshrrev_b32 v131, 22, v165
	v_bfe_u32 v132, v165, 21, 1
	v_lshl_add_u32 v131, v131, 2, v128
	v_mad_u32_u24 v132, v132, s1, 1
	ds_add_u32 v131, v132
	v_lshrrev_b32 v131, 22, v166
	v_bfe_u32 v132, v166, 21, 1
	v_lshl_add_u32 v131, v131, 2, v128
	v_mad_u32_u24 v132, v132, s1, 1
	ds_add_u32 v131, v132
	v_lshrrev_b32 v131, 22, v167
	v_bfe_u32 v132, v167, 21, 1
	v_lshl_add_u32 v131, v131, 2, v128
	v_mad_u32_u24 v132, v132, s1, 1
	ds_add_u32 v131, v132
	v_lshrrev_b32 v131, 22, v186
	v_bfe_u32 v123, v186, 21, 1
	v_mad_u32_u24 v123, v123, s1, 1
	v_lshl_add_u32 v131, v131, 2, v128
	ds_add_u32 v131, v123
	v_lshrrev_b32 v123, 22, v187
	v_bfe_u32 v124, v187, 21, 1
	v_lshl_add_u32 v123, v123, 2, v128
	v_mad_u32_u24 v124, v124, s1, 1
	ds_add_u32 v123, v124
	v_lshrrev_b32 v123, 22, v188
	v_bfe_u32 v124, v188, 21, 1
	v_lshl_add_u32 v123, v123, 2, v128
	v_mad_u32_u24 v124, v124, s1, 1
	ds_add_u32 v123, v124
	v_lshrrev_b32 v123, 22, v189
	v_bfe_u32 v124, v189, 21, 1
	v_lshl_add_u32 v123, v123, 2, v128
	v_mad_u32_u24 v124, v124, s1, 1
	ds_add_u32 v123, v124
	v_perm_b32 v216, v165, v164, v168
	v_perm_b32 v217, v166, v165, v169
	v_perm_b32 v218, v167, v166, v170
	v_perm_b32 v219, v187, v186, v168
	v_perm_b32 v220, v188, v187, v169
	v_perm_b32 v221, v189, v188, v170
	s_cmp_ge_i32 s15, s82
	s_cbranch_scc0 .LBB0_1308
	global_store_dwordx4 v232, v[216:219], s[20:21]
	global_store_dwordx2 v223, v[220:221], s[20:21]
	s_branch .LBB0_1310

.Lpb2_entry:
	s_waitcnt vmcnt(0)
	s_min_i32 s32, s82, s100
	v_mov_b32_e32 v235, 0xffff
	v_ashrrev_i32_e32 v196, 31, v139
	v_mov_b32_e32 v155, 0x0201000c
	v_mov_b32_e32 v168, 0x0504030c
	v_mov_b32_e32 v169, 0x0403020c
	v_mov_b32_e32 v170, 0x0302010c
	s_mul_i32 s85, s100, 0x600
	v_add_u32_e32 v234, s85, v230
	s_add_i32 s85, s31, 0
	s_min_i32 s85, s85, s100
	s_cmp_lt_i32 s85, 85
	s_cselect_b32 vcc_lo, s101, 0
	s_mul_i32 s85, s85, 0x600
	s_add_i32 s85, s85, vcc_lo
	v_add_u32_e32 v233, s85, v230
	v_add_u32_e32 v226, s85, v197
	global_load_dwordx4 v[156:159], v233, s[20:21]
	global_load_dwordx2 v[160:161], v226, s[20:21]
	global_store_dword v234, v193, s[20:21]
	s_add_i32 s85, s31, 8
	s_min_i32 s85, s85, s100
	s_cmp_lt_i32 s85, 85
	s_cselect_b32 vcc_lo, s101, 0
	s_mul_i32 s85, s85, 0x600
	s_add_i32 s85, s85, vcc_lo
	v_add_u32_e32 v233, s85, v230
	v_add_u32_e32 v226, s85, v197
	global_load_dwordx4 v[178:181], v233, s[20:21]
	global_load_dwordx2 v[182:183], v226, s[20:21]
	global_store_dword v234, v193, s[20:21]
	s_add_i32 s85, s31, 16
	s_min_i32 s85, s85, s100
	s_cmp_lt_i32 s85, 85
	s_cselect_b32 vcc_lo, s101, 0
	s_mul_i32 s85, s85, 0x600
	s_add_i32 s85, s85, vcc_lo
	v_add_u32_e32 v233, s85, v230
	v_add_u32_e32 v226, s85, v197
	global_load_dwordx4 v[236:239], v233, s[20:21]
	global_load_dwordx2 v[240:241], v226, s[20:21]
	global_store_dword v234, v193, s[20:21]
	s_add_i32 s85, s31, 24
	s_min_i32 s85, s85, s100
	s_cmp_lt_i32 s85, 85
	s_cselect_b32 vcc_lo, s101, 0
	s_mul_i32 s85, s85, 0x600
	s_add_i32 s85, s85, vcc_lo
	v_add_u32_e32 v233, s85, v230
	v_add_u32_e32 v226, s85, v197
	global_load_dwordx4 v[80:83], v233, s[20:21]
	global_load_dwordx2 v[84:85], v226, s[20:21]
	global_store_dword v234, v193, s[20:21]
.Lpb2_i0:
	s_add_i32 s85, s31, 32
	s_min_i32 s85, s85, s100
	s_cmp_lt_i32 s85, 85
	s_cselect_b32 vcc_lo, s101, 0
	s_mul_i32 s85, s85, 0x600
	s_add_i32 s85, s85, vcc_lo
	v_add_u32_e32 v233, s85, v230
	v_add_u32_e32 v226, s85, v197
	global_load_dwordx4 v[72:75], v233, s[20:21]
	global_load_dwordx2 v[76:77], v226, s[20:21]
	s_waitcnt vmcnt(12)
	v_perm_b32 v164, v156, v156, v155
	v_perm_b32 v165, v157, v156, v168
	v_perm_b32 v166, v158, v157, v169
	v_perm_b32 v167, v158, v158, v170
	v_perm_b32 v186, v159, v159, v155
	v_perm_b32 v187, v160, v159, v168
	v_perm_b32 v188, v161, v160, v169
	v_perm_b32 v189, v161, v161, v170
	v_cmp_ge_f32_e64 s[66:67], v164, v140
	v_cmp_ge_f32_e64 s[50:51], v164, v139
	v_cmp_ge_f32_e32 vcc, v165, v140
	v_cmp_ge_f32_e64 s[52:53], v165, v139
	v_cndmask_b32_e64 v224, 0, 1, s[66:67]
	v_cndmask_b32_e64 v225, 0, 2, vcc
	s_andn2_b64 s[50:51], s[50:51], s[66:67]
	s_andn2_b64 s[52:53], s[52:53], vcc
	v_or_b32_e32 v228, v224, v225
	v_cmp_ge_f32_e64 s[66:67], v166, v140
	v_cmp_ge_f32_e64 s[54:55], v166, v139
	v_cmp_ge_f32_e32 vcc, v167, v140
	v_cmp_ge_f32_e64 s[56:57], v167, v139
	v_cndmask_b32_e64 v224, 0, 4, s[66:67]
	v_cndmask_b32_e64 v225, 0, 8, vcc
	s_andn2_b64 s[54:55], s[54:55], s[66:67]
	s_andn2_b64 s[56:57], s[56:57], vcc
	v_or3_b32 v228, v228, v224, v225
	v_cmp_ge_f32_e64 s[66:67], v186, v140
	v_cmp_ge_f32_e64 s[58:59], v186, v139
	v_cmp_ge_f32_e32 vcc, v187, v140
	v_cmp_ge_f32_e64 s[60:61], v187, v139
	v_cndmask_b32_e64 v224, 0, v201, s[66:67]
	v_cndmask_b32_e64 v225, 0, v200, vcc
	s_andn2_b64 s[58:59], s[58:59], s[66:67]
	s_andn2_b64 s[60:61], s[60:61], vcc
	v_or3_b32 v228, v228, v224, v225
	v_cmp_ge_f32_e64 s[66:67], v188, v140
	v_cmp_ge_f32_e64 s[62:63], v188, v139
	v_cmp_ge_f32_e32 vcc, v189, v140
	v_cmp_ge_f32_e64 s[64:65], v189, v139
	v_cndmask_b32_e64 v224, 0, v199, s[66:67]
	v_cndmask_b32_e64 v225, 0, v198, vcc
	s_andn2_b64 s[62:63], s[62:63], s[66:67]
	s_andn2_b64 s[64:65], s[64:65], vcc
	v_or3_b32 v228, v228, v224, v225
	v_lshlrev_b32_e32 v104, v143, v228
	ds_bpermute_b32 v105, v144, v104
	v_mov_b32_e32 v227, s96
	s_mov_b64 s[14:15], exec
	s_mov_b64 exec, s[50:51]
	ds_add_rtn_u32 v214, v142, v193
	s_mov_b64 exec, s[52:53]
	ds_add_rtn_u32 v215, v142, v193
	s_mov_b64 exec, s[54:55]
	ds_add_rtn_u32 v216, v142, v193
	s_mov_b64 exec, s[56:57]
	ds_add_rtn_u32 v217, v142, v193
	s_mov_b64 exec, s[58:59]
	ds_add_rtn_u32 v218, v142, v193
	s_mov_b64 exec, s[60:61]
	ds_add_rtn_u32 v219, v142, v193
	s_mov_b64 exec, s[62:63]
	ds_add_rtn_u32 v220, v142, v193
	s_mov_b64 exec, s[64:65]
	ds_add_rtn_u32 v221, v142, v193
	s_mov_b64 exec, s[50:51]
	v_xor_b32_e32 v206, v196, v164
	v_bfe_u32 v222, v206, 11, 10
	v_bfe_u32 v223, v206, 10, 1
	v_lshl_add_u32 v222, v222, 2, v128
	v_mad_u32_u24 v223, v223, v235, 1
	ds_add_u32 v222, v223
	s_mov_b64 exec, s[52:53]
	v_xor_b32_e32 v207, v196, v165
	v_bfe_u32 v222, v207, 11, 10
	v_bfe_u32 v223, v207, 10, 1
	v_lshl_add_u32 v222, v222, 2, v128
	v_mad_u32_u24 v223, v223, v235, 1
	ds_add_u32 v222, v223
	s_mov_b64 exec, s[54:55]
	v_xor_b32_e32 v208, v196, v166
	v_bfe_u32 v222, v208, 11, 10
	v_bfe_u32 v223, v208, 10, 1
	v_lshl_add_u32 v222, v222, 2, v128
	v_mad_u32_u24 v223, v223, v235, 1
	ds_add_u32 v222, v223
	s_mov_b64 exec, s[56:57]
	v_xor_b32_e32 v209, v196, v167
	v_bfe_u32 v222, v209, 11, 10
	v_bfe_u32 v223, v209, 10, 1
	v_lshl_add_u32 v222, v222, 2, v128
	v_mad_u32_u24 v223, v223, v235, 1
	ds_add_u32 v222, v223
	s_waitcnt lgkmcnt(8)
	s_mov_b64 exec, s[58:59]
	v_xor_b32_e32 v210, v196, v186
	v_bfe_u32 v222, v210, 11, 10
	v_bfe_u32 v223, v210, 10, 1
	v_lshl_add_u32 v222, v222, 2, v128
	v_mad_u32_u24 v223, v223, v235, 1
	ds_add_u32 v222, v223
	s_mov_b64 exec, s[60:61]
	v_xor_b32_e32 v211, v196, v187
	v_bfe_u32 v222, v211, 11, 10
	v_bfe_u32 v223, v211, 10, 1
	v_lshl_add_u32 v222, v222, 2, v128
	v_mad_u32_u24 v223, v223, v235, 1
	ds_add_u32 v222, v223
	s_mov_b64 exec, s[62:63]
	v_xor_b32_e32 v212, v196, v188
	v_bfe_u32 v222, v212, 11, 10
	v_bfe_u32 v223, v212, 10, 1
	v_lshl_add_u32 v222, v222, 2, v128
	v_mad_u32_u24 v223, v223, v235, 1
	ds_add_u32 v222, v223
	s_mov_b64 exec, s[64:65]
	v_xor_b32_e32 v213, v196, v189
	v_bfe_u32 v222, v213, 11, 10
	v_bfe_u32 v223, v213, 10, 1
	v_lshl_add_u32 v222, v222, 2, v128
	v_mad_u32_u24 v223, v223, v235, 1
	ds_add_u32 v222, v223
	s_waitcnt lgkmcnt(8)
	s_mov_b64 exec, s[14:15]
	v_or_b32_e32 v104, v105, v104
	ds_bpermute_b32 v105, v145, v104
	s_mov_b64 exec, s[50:51]
	v_cmp_lt_u32_e64 s[66:67], s0, v214
	s_add_i32 s85, s74, 0x0
	v_bfe_u32 v224, v206, 10, 11
	v_lshl_add_u32 v222, v214, 2, v141
	v_add3_u32 v224, v224, v124, s85
	s_andn2_b64 exec, exec, s[66:67]
	ds_write_b32 v222, v224
	s_mov_b64 exec, s[66:67]
	ds_write_b32 v227, v193
	s_mov_b64 exec, s[52:53]
	v_cmp_lt_u32_e64 s[66:67], s0, v215
	s_add_i32 s85, s74, 0x800
	v_bfe_u32 v224, v207, 10, 11
	v_lshl_add_u32 v222, v215, 2, v141
	v_add3_u32 v224, v224, v124, s85
	s_andn2_b64 exec, exec, s[66:67]
	ds_write_b32 v222, v224
	s_mov_b64 exec, s[66:67]
	ds_write_b32 v227, v193
	s_waitcnt lgkmcnt(8)
	s_mov_b64 exec, s[54:55]
	v_cmp_lt_u32_e64 s[66:67], s0, v216
	s_add_i32 s85, s74, 0x1000
	v_bfe_u32 v224, v208, 10, 11
	v_lshl_add_u32 v222, v216, 2, v141
	v_add3_u32 v224, v224, v124, s85
	s_andn2_b64 exec, exec, s[66:67]
	ds_write_b32 v222, v224
	s_mov_b64 exec, s[66:67]
	ds_write_b32 v227, v193
	s_mov_b64 exec, s[56:57]
	v_cmp_lt_u32_e64 s[66:67], s0, v217
	s_add_i32 s85, s74, 0x1800
	v_bfe_u32 v224, v209, 10, 11
	v_lshl_add_u32 v222, v217, 2, v141
	v_add3_u32 v224, v224, v124, s85
	s_andn2_b64 exec, exec, s[66:67]
	ds_write_b32 v222, v224
	s_mov_b64 exec, s[66:67]
	ds_write_b32 v227, v193
	s_waitcnt lgkmcnt(8)
	s_mov_b64 exec, s[58:59]
	v_cmp_lt_u32_e64 s[66:67], s0, v218
	s_add_i32 s85, s74, 0x8000
	v_bfe_u32 v224, v210, 10, 11
	v_lshl_add_u32 v222, v218, 2, v141
	v_add3_u32 v224, v224, v124, s85
	s_andn2_b64 exec, exec, s[66:67]
	ds_write_b32 v222, v224
	s_mov_b64 exec, s[66:67]
	ds_write_b32 v227, v193
	s_mov_b64 exec, s[60:61]
	v_cmp_lt_u32_e64 s[66:67], s0, v219
	s_add_i32 s85, s74, 0x8800
	v_bfe_u32 v224, v211, 10, 11
	v_lshl_add_u32 v222, v219, 2, v141
	v_add3_u32 v224, v224, v124, s85
	s_andn2_b64 exec, exec, s[66:67]
	ds_write_b32 v222, v224
	s_mov_b64 exec, s[66:67]
	ds_write_b32 v227, v193
	s_waitcnt lgkmcnt(8)
	s_mov_b64 exec, s[62:63]
	v_cmp_lt_u32_e64 s[66:67], s0, v220
	s_add_i32 s85, s74, 0x9000
	v_bfe_u32 v224, v212, 10, 11
	v_lshl_add_u32 v222, v220, 2, v141
	v_add3_u32 v224, v224, v124, s85
	s_andn2_b64 exec, exec, s[66:67]
	ds_write_b32 v222, v224
	s_mov_b64 exec, s[66:67]
	ds_write_b32 v227, v193
	s_mov_b64 exec, s[64:65]
	v_cmp_lt_u32_e64 s[66:67], s0, v221
	s_add_i32 s85, s74, 0x9800
	v_bfe_u32 v224, v213, 10, 11
	v_lshl_add_u32 v222, v221, 2, v141
	v_add3_u32 v224, v224, v124, s85
	s_andn2_b64 exec, exec, s[66:67]
	ds_write_b32 v222, v224
	s_mov_b64 exec, s[66:67]
	ds_write_b32 v227, v193
	s_mov_b64 exec, s[14:15]
	s_and_saveexec_b64 s[14:15], s[38:39]
	v_or_b32_e32 v106, v104, v105
	v_lshl_add_u64 v[104:105], v[122:123], 0, s[74:75]
	v_add_co_u32_e32 v104, vcc, 0x3f700000, v104
	s_nop 1
	v_addc_co_u32_e32 v105, vcc, 0, v105, vcc
	global_store_dword v[104:105], v106, off
	s_or_b64 exec, exec, s[14:15]
	s_add_u32 s74, s74, 0x80000
	s_addc_u32 s75, s75, 0
	s_add_i32 s31, s31, 8
	s_cmp_ge_i32 s31, s32
	s_cbranch_scc1 .Lpb2_done
.Lpb2_i1:
	s_add_i32 s85, s31, 32
	s_min_i32 s85, s85, s100
	s_cmp_lt_i32 s85, 85
	s_cselect_b32 vcc_lo, s101, 0
	s_mul_i32 s85, s85, 0x600
	s_add_i32 s85, s85, vcc_lo
	v_add_u32_e32 v233, s85, v230
	v_add_u32_e32 v226, s85, v197
	global_load_dwordx4 v[156:159], v233, s[20:21]
	global_load_dwordx2 v[160:161], v226, s[20:21]
	s_waitcnt vmcnt(12)
	v_perm_b32 v164, v178, v178, v155
	v_perm_b32 v165, v179, v178, v168
	v_perm_b32 v166, v180, v179, v169
	v_perm_b32 v167, v180, v180, v170
	v_perm_b32 v186, v181, v181, v155
	v_perm_b32 v187, v182, v181, v168
	v_perm_b32 v188, v183, v182, v169
	v_perm_b32 v189, v183, v183, v170
	v_cmp_ge_f32_e64 s[66:67], v164, v140
	v_cmp_ge_f32_e64 s[50:51], v164, v139
	v_cmp_ge_f32_e32 vcc, v165, v140
	v_cmp_ge_f32_e64 s[52:53], v165, v139
	v_cndmask_b32_e64 v224, 0, 1, s[66:67]
	v_cndmask_b32_e64 v225, 0, 2, vcc
	s_andn2_b64 s[50:51], s[50:51], s[66:67]
	s_andn2_b64 s[52:53], s[52:53], vcc
	v_or_b32_e32 v228, v224, v225
	v_cmp_ge_f32_e64 s[66:67], v166, v140
	v_cmp_ge_f32_e64 s[54:55], v166, v139
	v_cmp_ge_f32_e32 vcc, v167, v140
	v_cmp_ge_f32_e64 s[56:57], v167, v139
	v_cndmask_b32_e64 v224, 0, 4, s[66:67]
	v_cndmask_b32_e64 v225, 0, 8, vcc
	s_andn2_b64 s[54:55], s[54:55], s[66:67]
	s_andn2_b64 s[56:57], s[56:57], vcc
	v_or3_b32 v228, v228, v224, v225
	v_cmp_ge_f32_e64 s[66:67], v186, v140
	v_cmp_ge_f32_e64 s[58:59], v186, v139
	v_cmp_ge_f32_e32 vcc, v187, v140
	v_cmp_ge_f32_e64 s[60:61], v187, v139
	v_cndmask_b32_e64 v224, 0, v201, s[66:67]
	v_cndmask_b32_e64 v225, 0, v200, vcc
	s_andn2_b64 s[58:59], s[58:59], s[66:67]
	s_andn2_b64 s[60:61], s[60:61], vcc
	v_or3_b32 v228, v228, v224, v225
	v_cmp_ge_f32_e64 s[66:67], v188, v140
	v_cmp_ge_f32_e64 s[62:63], v188, v139
	v_cmp_ge_f32_e32 vcc, v189, v140
	v_cmp_ge_f32_e64 s[64:65], v189, v139
	v_cndmask_b32_e64 v224, 0, v199, s[66:67]
	v_cndmask_b32_e64 v225, 0, v198, vcc
	s_andn2_b64 s[62:63], s[62:63], s[66:67]
	s_andn2_b64 s[64:65], s[64:65], vcc
	v_or3_b32 v228, v228, v224, v225
	v_lshlrev_b32_e32 v104, v143, v228
	ds_bpermute_b32 v105, v144, v104
	v_mov_b32_e32 v227, s96
	s_mov_b64 s[14:15], exec
	s_mov_b64 exec, s[50:51]
	ds_add_rtn_u32 v214, v142, v193
	s_mov_b64 exec, s[52:53]
	ds_add_rtn_u32 v215, v142, v193
	s_mov_b64 exec, s[54:55]
	ds_add_rtn_u32 v216, v142, v193
	s_mov_b64 exec, s[56:57]
	ds_add_rtn_u32 v217, v142, v193
	s_mov_b64 exec, s[58:59]
	ds_add_rtn_u32 v218, v142, v193
	s_mov_b64 exec, s[60:61]
	ds_add_rtn_u32 v219, v142, v193
	s_mov_b64 exec, s[62:63]
	ds_add_rtn_u32 v220, v142, v193
	s_mov_b64 exec, s[64:65]
	ds_add_rtn_u32 v221, v142, v193
	s_mov_b64 exec, s[50:51]
	v_xor_b32_e32 v206, v196, v164
	v_bfe_u32 v222, v206, 11, 10
	v_bfe_u32 v223, v206, 10, 1
	v_lshl_add_u32 v222, v222, 2, v128
	v_mad_u32_u24 v223, v223, v235, 1
	ds_add_u32 v222, v223
	s_mov_b64 exec, s[52:53]
	v_xor_b32_e32 v207, v196, v165
	v_bfe_u32 v222, v207, 11, 10
	v_bfe_u32 v223, v207, 10, 1
	v_lshl_add_u32 v222, v222, 2, v128
	v_mad_u32_u24 v223, v223, v235, 1
	ds_add_u32 v222, v223
	s_mov_b64 exec, s[54:55]
	v_xor_b32_e32 v208, v196, v166
	v_bfe_u32 v222, v208, 11, 10
	v_bfe_u32 v223, v208, 10, 1
	v_lshl_add_u32 v222, v222, 2, v128
	v_mad_u32_u24 v223, v223, v235, 1
	ds_add_u32 v222, v223
	s_mov_b64 exec, s[56:57]
	v_xor_b32_e32 v209, v196, v167
	v_bfe_u32 v222, v209, 11, 10
	v_bfe_u32 v223, v209, 10, 1
	v_lshl_add_u32 v222, v222, 2, v128
	v_mad_u32_u24 v223, v223, v235, 1
	ds_add_u32 v222, v223
	s_waitcnt lgkmcnt(8)
	s_mov_b64 exec, s[58:59]
	v_xor_b32_e32 v210, v196, v186
	v_bfe_u32 v222, v210, 11, 10
	v_bfe_u32 v223, v210, 10, 1
	v_lshl_add_u32 v222, v222, 2, v128
	v_mad_u32_u24 v223, v223, v235, 1
	ds_add_u32 v222, v223
	s_mov_b64 exec, s[60:61]
	v_xor_b32_e32 v211, v196, v187
	v_bfe_u32 v222, v211, 11, 10
	v_bfe_u32 v223, v211, 10, 1
	v_lshl_add_u32 v222, v222, 2, v128
	v_mad_u32_u24 v223, v223, v235, 1
	ds_add_u32 v222, v223
	s_mov_b64 exec, s[62:63]
	v_xor_b32_e32 v212, v196, v188
	v_bfe_u32 v222, v212, 11, 10
	v_bfe_u32 v223, v212, 10, 1
	v_lshl_add_u32 v222, v222, 2, v128
	v_mad_u32_u24 v223, v223, v235, 1
	ds_add_u32 v222, v223
	s_mov_b64 exec, s[64:65]
	v_xor_b32_e32 v213, v196, v189
	v_bfe_u32 v222, v213, 11, 10
	v_bfe_u32 v223, v213, 10, 1
	v_lshl_add_u32 v222, v222, 2, v128
	v_mad_u32_u24 v223, v223, v235, 1
	ds_add_u32 v222, v223
	s_waitcnt lgkmcnt(8)
	s_mov_b64 exec, s[14:15]
	v_or_b32_e32 v104, v105, v104
	ds_bpermute_b32 v105, v145, v104
	s_mov_b64 exec, s[50:51]
	v_cmp_lt_u32_e64 s[66:67], s0, v214
	s_add_i32 s85, s74, 0x0
	v_bfe_u32 v224, v206, 10, 11
	v_lshl_add_u32 v222, v214, 2, v141
	v_add3_u32 v224, v224, v124, s85
	s_andn2_b64 exec, exec, s[66:67]
	ds_write_b32 v222, v224
	s_mov_b64 exec, s[66:67]
	ds_write_b32 v227, v193
	s_mov_b64 exec, s[52:53]
	v_cmp_lt_u32_e64 s[66:67], s0, v215
	s_add_i32 s85, s74, 0x800
	v_bfe_u32 v224, v207, 10, 11
	v_lshl_add_u32 v222, v215, 2, v141
	v_add3_u32 v224, v224, v124, s85
	s_andn2_b64 exec, exec, s[66:67]
	ds_write_b32 v222, v224
	s_mov_b64 exec, s[66:67]
	ds_write_b32 v227, v193
	s_waitcnt lgkmcnt(8)
	s_mov_b64 exec, s[54:55]
	v_cmp_lt_u32_e64 s[66:67], s0, v216
	s_add_i32 s85, s74, 0x1000
	v_bfe_u32 v224, v208, 10, 11
	v_lshl_add_u32 v222, v216, 2, v141
	v_add3_u32 v224, v224, v124, s85
	s_andn2_b64 exec, exec, s[66:67]
	ds_write_b32 v222, v224
	s_mov_b64 exec, s[66:67]
	ds_write_b32 v227, v193
	s_mov_b64 exec, s[56:57]
	v_cmp_lt_u32_e64 s[66:67], s0, v217
	s_add_i32 s85, s74, 0x1800
	v_bfe_u32 v224, v209, 10, 11
	v_lshl_add_u32 v222, v217, 2, v141
	v_add3_u32 v224, v224, v124, s85
	s_andn2_b64 exec, exec, s[66:67]
	ds_write_b32 v222, v224
	s_mov_b64 exec, s[66:67]
	ds_write_b32 v227, v193
	s_waitcnt lgkmcnt(8)
	s_mov_b64 exec, s[58:59]
	v_cmp_lt_u32_e64 s[66:67], s0, v218
	s_add_i32 s85, s74, 0x8000
	v_bfe_u32 v224, v210, 10, 11
	v_lshl_add_u32 v222, v218, 2, v141
	v_add3_u32 v224, v224, v124, s85
	s_andn2_b64 exec, exec, s[66:67]
	ds_write_b32 v222, v224
	s_mov_b64 exec, s[66:67]
	ds_write_b32 v227, v193
	s_mov_b64 exec, s[60:61]
	v_cmp_lt_u32_e64 s[66:67], s0, v219
	s_add_i32 s85, s74, 0x8800
	v_bfe_u32 v224, v211, 10, 11
	v_lshl_add_u32 v222, v219, 2, v141
	v_add3_u32 v224, v224, v124, s85
	s_andn2_b64 exec, exec, s[66:67]
	ds_write_b32 v222, v224
	s_mov_b64 exec, s[66:67]
	ds_write_b32 v227, v193
	s_waitcnt lgkmcnt(8)
	s_mov_b64 exec, s[62:63]
	v_cmp_lt_u32_e64 s[66:67], s0, v220
	s_add_i32 s85, s74, 0x9000
	v_bfe_u32 v224, v212, 10, 11
	v_lshl_add_u32 v222, v220, 2, v141
	v_add3_u32 v224, v224, v124, s85
	s_andn2_b64 exec, exec, s[66:67]
	ds_write_b32 v222, v224
	s_mov_b64 exec, s[66:67]
	ds_write_b32 v227, v193
	s_mov_b64 exec, s[64:65]
	v_cmp_lt_u32_e64 s[66:67], s0, v221
	s_add_i32 s85, s74, 0x9800
	v_bfe_u32 v224, v213, 10, 11
	v_lshl_add_u32 v222, v221, 2, v141
	v_add3_u32 v224, v224, v124, s85
	s_andn2_b64 exec, exec, s[66:67]
	ds_write_b32 v222, v224
	s_mov_b64 exec, s[66:67]
	ds_write_b32 v227, v193
	s_mov_b64 exec, s[14:15]
	s_and_saveexec_b64 s[14:15], s[38:39]
	v_or_b32_e32 v106, v104, v105
	v_lshl_add_u64 v[104:105], v[122:123], 0, s[74:75]
	v_add_co_u32_e32 v104, vcc, 0x3f700000, v104
	s_nop 1
	v_addc_co_u32_e32 v105, vcc, 0, v105, vcc
	global_store_dword v[104:105], v106, off
	s_or_b64 exec, exec, s[14:15]
	s_add_u32 s74, s74, 0x80000
	s_addc_u32 s75, s75, 0
	s_add_i32 s31, s31, 8
	s_cmp_ge_i32 s31, s32
	s_cbranch_scc1 .Lpb2_done
.Lpb2_i2:
	s_add_i32 s85, s31, 32
	s_min_i32 s85, s85, s100
	s_cmp_lt_i32 s85, 85
	s_cselect_b32 vcc_lo, s101, 0
	s_mul_i32 s85, s85, 0x600
	s_add_i32 s85, s85, vcc_lo
	v_add_u32_e32 v233, s85, v230
	v_add_u32_e32 v226, s85, v197
	global_load_dwordx4 v[178:181], v233, s[20:21]
	global_load_dwordx2 v[182:183], v226, s[20:21]
	s_waitcnt vmcnt(12)
	v_perm_b32 v164, v236, v236, v155
	v_perm_b32 v165, v237, v236, v168
	v_perm_b32 v166, v238, v237, v169
	v_perm_b32 v167, v238, v238, v170
	v_perm_b32 v186, v239, v239, v155
	v_perm_b32 v187, v240, v239, v168
	v_perm_b32 v188, v241, v240, v169
	v_perm_b32 v189, v241, v241, v170
	v_cmp_ge_f32_e64 s[66:67], v164, v140
	v_cmp_ge_f32_e64 s[50:51], v164, v139
	v_cmp_ge_f32_e32 vcc, v165, v140
	v_cmp_ge_f32_e64 s[52:53], v165, v139
	v_cndmask_b32_e64 v224, 0, 1, s[66:67]
	v_cndmask_b32_e64 v225, 0, 2, vcc
	s_andn2_b64 s[50:51], s[50:51], s[66:67]
	s_andn2_b64 s[52:53], s[52:53], vcc
	v_or_b32_e32 v228, v224, v225
	v_cmp_ge_f32_e64 s[66:67], v166, v140
	v_cmp_ge_f32_e64 s[54:55], v166, v139
	v_cmp_ge_f32_e32 vcc, v167, v140
	v_cmp_ge_f32_e64 s[56:57], v167, v139
	v_cndmask_b32_e64 v224, 0, 4, s[66:67]
	v_cndmask_b32_e64 v225, 0, 8, vcc
	s_andn2_b64 s[54:55], s[54:55], s[66:67]
	s_andn2_b64 s[56:57], s[56:57], vcc
	v_or3_b32 v228, v228, v224, v225
	v_cmp_ge_f32_e64 s[66:67], v186, v140
	v_cmp_ge_f32_e64 s[58:59], v186, v139
	v_cmp_ge_f32_e32 vcc, v187, v140
	v_cmp_ge_f32_e64 s[60:61], v187, v139
	v_cndmask_b32_e64 v224, 0, v201, s[66:67]
	v_cndmask_b32_e64 v225, 0, v200, vcc
	s_andn2_b64 s[58:59], s[58:59], s[66:67]
	s_andn2_b64 s[60:61], s[60:61], vcc
	v_or3_b32 v228, v228, v224, v225
	v_cmp_ge_f32_e64 s[66:67], v188, v140
	v_cmp_ge_f32_e64 s[62:63], v188, v139
	v_cmp_ge_f32_e32 vcc, v189, v140
	v_cmp_ge_f32_e64 s[64:65], v189, v139
	v_cndmask_b32_e64 v224, 0, v199, s[66:67]
	v_cndmask_b32_e64 v225, 0, v198, vcc
	s_andn2_b64 s[62:63], s[62:63], s[66:67]
	s_andn2_b64 s[64:65], s[64:65], vcc
	v_or3_b32 v228, v228, v224, v225
	v_lshlrev_b32_e32 v104, v143, v228
	ds_bpermute_b32 v105, v144, v104
	v_mov_b32_e32 v227, s96
	s_mov_b64 s[14:15], exec
	s_mov_b64 exec, s[50:51]
	ds_add_rtn_u32 v214, v142, v193
	s_mov_b64 exec, s[52:53]
	ds_add_rtn_u32 v215, v142, v193
	s_mov_b64 exec, s[54:55]
	ds_add_rtn_u32 v216, v142, v193
	s_mov_b64 exec, s[56:57]
	ds_add_rtn_u32 v217, v142, v193
	s_mov_b64 exec, s[58:59]
	ds_add_rtn_u32 v218, v142, v193
	s_mov_b64 exec, s[60:61]
	ds_add_rtn_u32 v219, v142, v193
	s_mov_b64 exec, s[62:63]
	ds_add_rtn_u32 v220, v142, v193
	s_mov_b64 exec, s[64:65]
	ds_add_rtn_u32 v221, v142, v193
	s_mov_b64 exec, s[50:51]
	v_xor_b32_e32 v206, v196, v164
	v_bfe_u32 v222, v206, 11, 10
	v_bfe_u32 v223, v206, 10, 1
	v_lshl_add_u32 v222, v222, 2, v128
	v_mad_u32_u24 v223, v223, v235, 1
	ds_add_u32 v222, v223
	s_mov_b64 exec, s[52:53]
	v_xor_b32_e32 v207, v196, v165
	v_bfe_u32 v222, v207, 11, 10
	v_bfe_u32 v223, v207, 10, 1
	v_lshl_add_u32 v222, v222, 2, v128
	v_mad_u32_u24 v223, v223, v235, 1
	ds_add_u32 v222, v223
	s_mov_b64 exec, s[54:55]
	v_xor_b32_e32 v208, v196, v166
	v_bfe_u32 v222, v208, 11, 10
	v_bfe_u32 v223, v208, 10, 1
	v_lshl_add_u32 v222, v222, 2, v128
	v_mad_u32_u24 v223, v223, v235, 1
	ds_add_u32 v222, v223
	s_mov_b64 exec, s[56:57]
	v_xor_b32_e32 v209, v196, v167
	v_bfe_u32 v222, v209, 11, 10
	v_bfe_u32 v223, v209, 10, 1
	v_lshl_add_u32 v222, v222, 2, v128
	v_mad_u32_u24 v223, v223, v235, 1
	ds_add_u32 v222, v223
	s_waitcnt lgkmcnt(8)
	s_mov_b64 exec, s[58:59]
	v_xor_b32_e32 v210, v196, v186
	v_bfe_u32 v222, v210, 11, 10
	v_bfe_u32 v223, v210, 10, 1
	v_lshl_add_u32 v222, v222, 2, v128
	v_mad_u32_u24 v223, v223, v235, 1
	ds_add_u32 v222, v223
	s_mov_b64 exec, s[60:61]
	v_xor_b32_e32 v211, v196, v187
	v_bfe_u32 v222, v211, 11, 10
	v_bfe_u32 v223, v211, 10, 1
	v_lshl_add_u32 v222, v222, 2, v128
	v_mad_u32_u24 v223, v223, v235, 1
	ds_add_u32 v222, v223
	s_mov_b64 exec, s[62:63]
	v_xor_b32_e32 v212, v196, v188
	v_bfe_u32 v222, v212, 11, 10
	v_bfe_u32 v223, v212, 10, 1
	v_lshl_add_u32 v222, v222, 2, v128
	v_mad_u32_u24 v223, v223, v235, 1
	ds_add_u32 v222, v223
	s_mov_b64 exec, s[64:65]
	v_xor_b32_e32 v213, v196, v189
	v_bfe_u32 v222, v213, 11, 10
	v_bfe_u32 v223, v213, 10, 1
	v_lshl_add_u32 v222, v222, 2, v128
	v_mad_u32_u24 v223, v223, v235, 1
	ds_add_u32 v222, v223
	s_waitcnt lgkmcnt(8)
	s_mov_b64 exec, s[14:15]
	v_or_b32_e32 v104, v105, v104
	ds_bpermute_b32 v105, v145, v104
	s_mov_b64 exec, s[50:51]
	v_cmp_lt_u32_e64 s[66:67], s0, v214
	s_add_i32 s85, s74, 0x0
	v_bfe_u32 v224, v206, 10, 11
	v_lshl_add_u32 v222, v214, 2, v141
	v_add3_u32 v224, v224, v124, s85
	s_andn2_b64 exec, exec, s[66:67]
	ds_write_b32 v222, v224
	s_mov_b64 exec, s[66:67]
	ds_write_b32 v227, v193
	s_mov_b64 exec, s[52:53]
	v_cmp_lt_u32_e64 s[66:67], s0, v215
	s_add_i32 s85, s74, 0x800
	v_bfe_u32 v224, v207, 10, 11
	v_lshl_add_u32 v222, v215, 2, v141
	v_add3_u32 v224, v224, v124, s85
	s_andn2_b64 exec, exec, s[66:67]
	ds_write_b32 v222, v224
	s_mov_b64 exec, s[66:67]
	ds_write_b32 v227, v193
	s_waitcnt lgkmcnt(8)
	s_mov_b64 exec, s[54:55]
	v_cmp_lt_u32_e64 s[66:67], s0, v216
	s_add_i32 s85, s74, 0x1000
	v_bfe_u32 v224, v208, 10, 11
	v_lshl_add_u32 v222, v216, 2, v141
	v_add3_u32 v224, v224, v124, s85
	s_andn2_b64 exec, exec, s[66:67]
	ds_write_b32 v222, v224
	s_mov_b64 exec, s[66:67]
	ds_write_b32 v227, v193
	s_mov_b64 exec, s[56:57]
	v_cmp_lt_u32_e64 s[66:67], s0, v217
	s_add_i32 s85, s74, 0x1800
	v_bfe_u32 v224, v209, 10, 11
	v_lshl_add_u32 v222, v217, 2, v141
	v_add3_u32 v224, v224, v124, s85
	s_andn2_b64 exec, exec, s[66:67]
	ds_write_b32 v222, v224
	s_mov_b64 exec, s[66:67]
	ds_write_b32 v227, v193
	s_waitcnt lgkmcnt(8)
	s_mov_b64 exec, s[58:59]
	v_cmp_lt_u32_e64 s[66:67], s0, v218
	s_add_i32 s85, s74, 0x8000
	v_bfe_u32 v224, v210, 10, 11
	v_lshl_add_u32 v222, v218, 2, v141
	v_add3_u32 v224, v224, v124, s85
	s_andn2_b64 exec, exec, s[66:67]
	ds_write_b32 v222, v224
	s_mov_b64 exec, s[66:67]
	ds_write_b32 v227, v193
	s_mov_b64 exec, s[60:61]
	v_cmp_lt_u32_e64 s[66:67], s0, v219
	s_add_i32 s85, s74, 0x8800
	v_bfe_u32 v224, v211, 10, 11
	v_lshl_add_u32 v222, v219, 2, v141
	v_add3_u32 v224, v224, v124, s85
	s_andn2_b64 exec, exec, s[66:67]
	ds_write_b32 v222, v224
	s_mov_b64 exec, s[66:67]
	ds_write_b32 v227, v193
	s_waitcnt lgkmcnt(8)
	s_mov_b64 exec, s[62:63]
	v_cmp_lt_u32_e64 s[66:67], s0, v220
	s_add_i32 s85, s74, 0x9000
	v_bfe_u32 v224, v212, 10, 11
	v_lshl_add_u32 v222, v220, 2, v141
	v_add3_u32 v224, v224, v124, s85
	s_andn2_b64 exec, exec, s[66:67]
	ds_write_b32 v222, v224
	s_mov_b64 exec, s[66:67]
	ds_write_b32 v227, v193
	s_mov_b64 exec, s[64:65]
	v_cmp_lt_u32_e64 s[66:67], s0, v221
	s_add_i32 s85, s74, 0x9800
	v_bfe_u32 v224, v213, 10, 11
	v_lshl_add_u32 v222, v221, 2, v141
	v_add3_u32 v224, v224, v124, s85
	s_andn2_b64 exec, exec, s[66:67]
	ds_write_b32 v222, v224
	s_mov_b64 exec, s[66:67]
	ds_write_b32 v227, v193
	s_mov_b64 exec, s[14:15]
	s_and_saveexec_b64 s[14:15], s[38:39]
	v_or_b32_e32 v106, v104, v105
	v_lshl_add_u64 v[104:105], v[122:123], 0, s[74:75]
	v_add_co_u32_e32 v104, vcc, 0x3f700000, v104
	s_nop 1
	v_addc_co_u32_e32 v105, vcc, 0, v105, vcc
	global_store_dword v[104:105], v106, off
	s_or_b64 exec, exec, s[14:15]
	s_add_u32 s74, s74, 0x80000
	s_addc_u32 s75, s75, 0
	s_add_i32 s31, s31, 8
	s_cmp_ge_i32 s31, s32
	s_cbranch_scc1 .Lpb2_done
.Lpb2_i3:
	s_add_i32 s85, s31, 32
	s_min_i32 s85, s85, s100
	s_cmp_lt_i32 s85, 85
	s_cselect_b32 vcc_lo, s101, 0
	s_mul_i32 s85, s85, 0x600
	s_add_i32 s85, s85, vcc_lo
	v_add_u32_e32 v233, s85, v230
	v_add_u32_e32 v226, s85, v197
	global_load_dwordx4 v[236:239], v233, s[20:21]
	global_load_dwordx2 v[240:241], v226, s[20:21]
	s_waitcnt vmcnt(12)
	v_perm_b32 v164, v80, v80, v155
	v_perm_b32 v165, v81, v80, v168
	v_perm_b32 v166, v82, v81, v169
	v_perm_b32 v167, v82, v82, v170
	v_perm_b32 v186, v83, v83, v155
	v_perm_b32 v187, v84, v83, v168
	v_perm_b32 v188, v85, v84, v169
	v_perm_b32 v189, v85, v85, v170
	v_cmp_ge_f32_e64 s[66:67], v164, v140
	v_cmp_ge_f32_e64 s[50:51], v164, v139
	v_cmp_ge_f32_e32 vcc, v165, v140
	v_cmp_ge_f32_e64 s[52:53], v165, v139
	v_cndmask_b32_e64 v224, 0, 1, s[66:67]
	v_cndmask_b32_e64 v225, 0, 2, vcc
	s_andn2_b64 s[50:51], s[50:51], s[66:67]
	s_andn2_b64 s[52:53], s[52:53], vcc
	v_or_b32_e32 v228, v224, v225
	v_cmp_ge_f32_e64 s[66:67], v166, v140
	v_cmp_ge_f32_e64 s[54:55], v166, v139
	v_cmp_ge_f32_e32 vcc, v167, v140
	v_cmp_ge_f32_e64 s[56:57], v167, v139
	v_cndmask_b32_e64 v224, 0, 4, s[66:67]
	v_cndmask_b32_e64 v225, 0, 8, vcc
	s_andn2_b64 s[54:55], s[54:55], s[66:67]
	s_andn2_b64 s[56:57], s[56:57], vcc
	v_or3_b32 v228, v228, v224, v225
	v_cmp_ge_f32_e64 s[66:67], v186, v140
	v_cmp_ge_f32_e64 s[58:59], v186, v139
	v_cmp_ge_f32_e32 vcc, v187, v140
	v_cmp_ge_f32_e64 s[60:61], v187, v139
	v_cndmask_b32_e64 v224, 0, v201, s[66:67]
	v_cndmask_b32_e64 v225, 0, v200, vcc
	s_andn2_b64 s[58:59], s[58:59], s[66:67]
	s_andn2_b64 s[60:61], s[60:61], vcc
	v_or3_b32 v228, v228, v224, v225
	v_cmp_ge_f32_e64 s[66:67], v188, v140
	v_cmp_ge_f32_e64 s[62:63], v188, v139
	v_cmp_ge_f32_e32 vcc, v189, v140
	v_cmp_ge_f32_e64 s[64:65], v189, v139
	v_cndmask_b32_e64 v224, 0, v199, s[66:67]
	v_cndmask_b32_e64 v225, 0, v198, vcc
	s_andn2_b64 s[62:63], s[62:63], s[66:67]
	s_andn2_b64 s[64:65], s[64:65], vcc
	v_or3_b32 v228, v228, v224, v225
	v_lshlrev_b32_e32 v104, v143, v228
	ds_bpermute_b32 v105, v144, v104
	v_mov_b32_e32 v227, s96
	s_mov_b64 s[14:15], exec
	s_mov_b64 exec, s[50:51]
	ds_add_rtn_u32 v214, v142, v193
	s_mov_b64 exec, s[52:53]
	ds_add_rtn_u32 v215, v142, v193
	s_mov_b64 exec, s[54:55]
	ds_add_rtn_u32 v216, v142, v193
	s_mov_b64 exec, s[56:57]
	ds_add_rtn_u32 v217, v142, v193
	s_mov_b64 exec, s[58:59]
	ds_add_rtn_u32 v218, v142, v193
	s_mov_b64 exec, s[60:61]
	ds_add_rtn_u32 v219, v142, v193
	s_mov_b64 exec, s[62:63]
	ds_add_rtn_u32 v220, v142, v193
	s_mov_b64 exec, s[64:65]
	ds_add_rtn_u32 v221, v142, v193
	s_mov_b64 exec, s[50:51]
	v_xor_b32_e32 v206, v196, v164
	v_bfe_u32 v222, v206, 11, 10
	v_bfe_u32 v223, v206, 10, 1
	v_lshl_add_u32 v222, v222, 2, v128
	v_mad_u32_u24 v223, v223, v235, 1
	ds_add_u32 v222, v223
	s_mov_b64 exec, s[52:53]
	v_xor_b32_e32 v207, v196, v165
	v_bfe_u32 v222, v207, 11, 10
	v_bfe_u32 v223, v207, 10, 1
	v_lshl_add_u32 v222, v222, 2, v128
	v_mad_u32_u24 v223, v223, v235, 1
	ds_add_u32 v222, v223
	s_mov_b64 exec, s[54:55]
	v_xor_b32_e32 v208, v196, v166
	v_bfe_u32 v222, v208, 11, 10
	v_bfe_u32 v223, v208, 10, 1
	v_lshl_add_u32 v222, v222, 2, v128
	v_mad_u32_u24 v223, v223, v235, 1
	ds_add_u32 v222, v223
	s_mov_b64 exec, s[56:57]
	v_xor_b32_e32 v209, v196, v167
	v_bfe_u32 v222, v209, 11, 10
	v_bfe_u32 v223, v209, 10, 1
	v_lshl_add_u32 v222, v222, 2, v128
	v_mad_u32_u24 v223, v223, v235, 1
	ds_add_u32 v222, v223
	s_waitcnt lgkmcnt(8)
	s_mov_b64 exec, s[58:59]
	v_xor_b32_e32 v210, v196, v186
	v_bfe_u32 v222, v210, 11, 10
	v_bfe_u32 v223, v210, 10, 1
	v_lshl_add_u32 v222, v222, 2, v128
	v_mad_u32_u24 v223, v223, v235, 1
	ds_add_u32 v222, v223
	s_mov_b64 exec, s[60:61]
	v_xor_b32_e32 v211, v196, v187
	v_bfe_u32 v222, v211, 11, 10
	v_bfe_u32 v223, v211, 10, 1
	v_lshl_add_u32 v222, v222, 2, v128
	v_mad_u32_u24 v223, v223, v235, 1
	ds_add_u32 v222, v223
	s_mov_b64 exec, s[62:63]
	v_xor_b32_e32 v212, v196, v188
	v_bfe_u32 v222, v212, 11, 10
	v_bfe_u32 v223, v212, 10, 1
	v_lshl_add_u32 v222, v222, 2, v128
	v_mad_u32_u24 v223, v223, v235, 1
	ds_add_u32 v222, v223
	s_mov_b64 exec, s[64:65]
	v_xor_b32_e32 v213, v196, v189
	v_bfe_u32 v222, v213, 11, 10
	v_bfe_u32 v223, v213, 10, 1
	v_lshl_add_u32 v222, v222, 2, v128
	v_mad_u32_u24 v223, v223, v235, 1
	ds_add_u32 v222, v223
	s_waitcnt lgkmcnt(8)
	s_mov_b64 exec, s[14:15]
	v_or_b32_e32 v104, v105, v104
	ds_bpermute_b32 v105, v145, v104
	s_mov_b64 exec, s[50:51]
	v_cmp_lt_u32_e64 s[66:67], s0, v214
	s_add_i32 s85, s74, 0x0
	v_bfe_u32 v224, v206, 10, 11
	v_lshl_add_u32 v222, v214, 2, v141
	v_add3_u32 v224, v224, v124, s85
	s_andn2_b64 exec, exec, s[66:67]
	ds_write_b32 v222, v224
	s_mov_b64 exec, s[66:67]
	ds_write_b32 v227, v193
	s_mov_b64 exec, s[52:53]
	v_cmp_lt_u32_e64 s[66:67], s0, v215
	s_add_i32 s85, s74, 0x800
	v_bfe_u32 v224, v207, 10, 11
	v_lshl_add_u32 v222, v215, 2, v141
	v_add3_u32 v224, v224, v124, s85
	s_andn2_b64 exec, exec, s[66:67]
	ds_write_b32 v222, v224
	s_mov_b64 exec, s[66:67]
	ds_write_b32 v227, v193
	s_waitcnt lgkmcnt(8)
	s_mov_b64 exec, s[54:55]
	v_cmp_lt_u32_e64 s[66:67], s0, v216
	s_add_i32 s85, s74, 0x1000
	v_bfe_u32 v224, v208, 10, 11
	v_lshl_add_u32 v222, v216, 2, v141
	v_add3_u32 v224, v224, v124, s85
	s_andn2_b64 exec, exec, s[66:67]
	ds_write_b32 v222, v224
	s_mov_b64 exec, s[66:67]
	ds_write_b32 v227, v193
	s_mov_b64 exec, s[56:57]
	v_cmp_lt_u32_e64 s[66:67], s0, v217
	s_add_i32 s85, s74, 0x1800
	v_bfe_u32 v224, v209, 10, 11
	v_lshl_add_u32 v222, v217, 2, v141
	v_add3_u32 v224, v224, v124, s85
	s_andn2_b64 exec, exec, s[66:67]
	ds_write_b32 v222, v224
	s_mov_b64 exec, s[66:67]
	ds_write_b32 v227, v193
	s_waitcnt lgkmcnt(8)
	s_mov_b64 exec, s[58:59]
	v_cmp_lt_u32_e64 s[66:67], s0, v218
	s_add_i32 s85, s74, 0x8000
	v_bfe_u32 v224, v210, 10, 11
	v_lshl_add_u32 v222, v218, 2, v141
	v_add3_u32 v224, v224, v124, s85
	s_andn2_b64 exec, exec, s[66:67]
	ds_write_b32 v222, v224
	s_mov_b64 exec, s[66:67]
	ds_write_b32 v227, v193
	s_mov_b64 exec, s[60:61]
	v_cmp_lt_u32_e64 s[66:67], s0, v219
	s_add_i32 s85, s74, 0x8800
	v_bfe_u32 v224, v211, 10, 11
	v_lshl_add_u32 v222, v219, 2, v141
	v_add3_u32 v224, v224, v124, s85
	s_andn2_b64 exec, exec, s[66:67]
	ds_write_b32 v222, v224
	s_mov_b64 exec, s[66:67]
	ds_write_b32 v227, v193
	s_waitcnt lgkmcnt(8)
	s_mov_b64 exec, s[62:63]
	v_cmp_lt_u32_e64 s[66:67], s0, v220
	s_add_i32 s85, s74, 0x9000
	v_bfe_u32 v224, v212, 10, 11
	v_lshl_add_u32 v222, v220, 2, v141
	v_add3_u32 v224, v224, v124, s85
	s_andn2_b64 exec, exec, s[66:67]
	ds_write_b32 v222, v224
	s_mov_b64 exec, s[66:67]
	ds_write_b32 v227, v193
	s_mov_b64 exec, s[64:65]
	v_cmp_lt_u32_e64 s[66:67], s0, v221
	s_add_i32 s85, s74, 0x9800
	v_bfe_u32 v224, v213, 10, 11
	v_lshl_add_u32 v222, v221, 2, v141
	v_add3_u32 v224, v224, v124, s85
	s_andn2_b64 exec, exec, s[66:67]
	ds_write_b32 v222, v224
	s_mov_b64 exec, s[66:67]
	ds_write_b32 v227, v193
	s_mov_b64 exec, s[14:15]
	s_and_saveexec_b64 s[14:15], s[38:39]
	v_or_b32_e32 v106, v104, v105
	v_lshl_add_u64 v[104:105], v[122:123], 0, s[74:75]
	v_add_co_u32_e32 v104, vcc, 0x3f700000, v104
	s_nop 1
	v_addc_co_u32_e32 v105, vcc, 0, v105, vcc
	global_store_dword v[104:105], v106, off
	s_or_b64 exec, exec, s[14:15]
	s_add_u32 s74, s74, 0x80000
	s_addc_u32 s75, s75, 0
	s_add_i32 s31, s31, 8
	s_cmp_ge_i32 s31, s32
	s_cbranch_scc1 .Lpb2_done
.Lpb2_i4:
	s_add_i32 s85, s31, 32
	s_min_i32 s85, s85, s100
	s_cmp_lt_i32 s85, 85
	s_cselect_b32 vcc_lo, s101, 0
	s_mul_i32 s85, s85, 0x600
	s_add_i32 s85, s85, vcc_lo
	v_add_u32_e32 v233, s85, v230
	v_add_u32_e32 v226, s85, v197
	global_load_dwordx4 v[80:83], v233, s[20:21]
	global_load_dwordx2 v[84:85], v226, s[20:21]
	s_waitcnt vmcnt(12)
	v_perm_b32 v164, v72, v72, v155
	v_perm_b32 v165, v73, v72, v168
	v_perm_b32 v166, v74, v73, v169
	v_perm_b32 v167, v74, v74, v170
	v_perm_b32 v186, v75, v75, v155
	v_perm_b32 v187, v76, v75, v168
	v_perm_b32 v188, v77, v76, v169
	v_perm_b32 v189, v77, v77, v170
	v_cmp_ge_f32_e64 s[66:67], v164, v140
	v_cmp_ge_f32_e64 s[50:51], v164, v139
	v_cmp_ge_f32_e32 vcc, v165, v140
	v_cmp_ge_f32_e64 s[52:53], v165, v139
	v_cndmask_b32_e64 v224, 0, 1, s[66:67]
	v_cndmask_b32_e64 v225, 0, 2, vcc
	s_andn2_b64 s[50:51], s[50:51], s[66:67]
	s_andn2_b64 s[52:53], s[52:53], vcc
	v_or_b32_e32 v228, v224, v225
	v_cmp_ge_f32_e64 s[66:67], v166, v140
	v_cmp_ge_f32_e64 s[54:55], v166, v139
	v_cmp_ge_f32_e32 vcc, v167, v140
	v_cmp_ge_f32_e64 s[56:57], v167, v139
	v_cndmask_b32_e64 v224, 0, 4, s[66:67]
	v_cndmask_b32_e64 v225, 0, 8, vcc
	s_andn2_b64 s[54:55], s[54:55], s[66:67]
	s_andn2_b64 s[56:57], s[56:57], vcc
	v_or3_b32 v228, v228, v224, v225
	v_cmp_ge_f32_e64 s[66:67], v186, v140
	v_cmp_ge_f32_e64 s[58:59], v186, v139
	v_cmp_ge_f32_e32 vcc, v187, v140
	v_cmp_ge_f32_e64 s[60:61], v187, v139
	v_cndmask_b32_e64 v224, 0, v201, s[66:67]
	v_cndmask_b32_e64 v225, 0, v200, vcc
	s_andn2_b64 s[58:59], s[58:59], s[66:67]
	s_andn2_b64 s[60:61], s[60:61], vcc
	v_or3_b32 v228, v228, v224, v225
	v_cmp_ge_f32_e64 s[66:67], v188, v140
	v_cmp_ge_f32_e64 s[62:63], v188, v139
	v_cmp_ge_f32_e32 vcc, v189, v140
	v_cmp_ge_f32_e64 s[64:65], v189, v139
	v_cndmask_b32_e64 v224, 0, v199, s[66:67]
	v_cndmask_b32_e64 v225, 0, v198, vcc
	s_andn2_b64 s[62:63], s[62:63], s[66:67]
	s_andn2_b64 s[64:65], s[64:65], vcc
	v_or3_b32 v228, v228, v224, v225
	v_lshlrev_b32_e32 v104, v143, v228
	ds_bpermute_b32 v105, v144, v104
	v_mov_b32_e32 v227, s96
	s_mov_b64 s[14:15], exec
	s_mov_b64 exec, s[50:51]
	ds_add_rtn_u32 v214, v142, v193
	s_mov_b64 exec, s[52:53]
	ds_add_rtn_u32 v215, v142, v193
	s_mov_b64 exec, s[54:55]
	ds_add_rtn_u32 v216, v142, v193
	s_mov_b64 exec, s[56:57]
	ds_add_rtn_u32 v217, v142, v193
	s_mov_b64 exec, s[58:59]
	ds_add_rtn_u32 v218, v142, v193
	s_mov_b64 exec, s[60:61]
	ds_add_rtn_u32 v219, v142, v193
	s_mov_b64 exec, s[62:63]
	ds_add_rtn_u32 v220, v142, v193
	s_mov_b64 exec, s[64:65]
	ds_add_rtn_u32 v221, v142, v193
	s_mov_b64 exec, s[50:51]
	v_xor_b32_e32 v206, v196, v164
	v_bfe_u32 v222, v206, 11, 10
	v_bfe_u32 v223, v206, 10, 1
	v_lshl_add_u32 v222, v222, 2, v128
	v_mad_u32_u24 v223, v223, v235, 1
	ds_add_u32 v222, v223
	s_mov_b64 exec, s[52:53]
	v_xor_b32_e32 v207, v196, v165
	v_bfe_u32 v222, v207, 11, 10
	v_bfe_u32 v223, v207, 10, 1
	v_lshl_add_u32 v222, v222, 2, v128
	v_mad_u32_u24 v223, v223, v235, 1
	ds_add_u32 v222, v223
	s_mov_b64 exec, s[54:55]
	v_xor_b32_e32 v208, v196, v166
	v_bfe_u32 v222, v208, 11, 10
	v_bfe_u32 v223, v208, 10, 1
	v_lshl_add_u32 v222, v222, 2, v128
	v_mad_u32_u24 v223, v223, v235, 1
	ds_add_u32 v222, v223
	s_mov_b64 exec, s[56:57]
	v_xor_b32_e32 v209, v196, v167
	v_bfe_u32 v222, v209, 11, 10
	v_bfe_u32 v223, v209, 10, 1
	v_lshl_add_u32 v222, v222, 2, v128
	v_mad_u32_u24 v223, v223, v235, 1
	ds_add_u32 v222, v223
	s_waitcnt lgkmcnt(8)
	s_mov_b64 exec, s[58:59]
	v_xor_b32_e32 v210, v196, v186
	v_bfe_u32 v222, v210, 11, 10
	v_bfe_u32 v223, v210, 10, 1
	v_lshl_add_u32 v222, v222, 2, v128
	v_mad_u32_u24 v223, v223, v235, 1
	ds_add_u32 v222, v223
	s_mov_b64 exec, s[60:61]
	v_xor_b32_e32 v211, v196, v187
	v_bfe_u32 v222, v211, 11, 10
	v_bfe_u32 v223, v211, 10, 1
	v_lshl_add_u32 v222, v222, 2, v128
	v_mad_u32_u24 v223, v223, v235, 1
	ds_add_u32 v222, v223
	s_mov_b64 exec, s[62:63]
	v_xor_b32_e32 v212, v196, v188
	v_bfe_u32 v222, v212, 11, 10
	v_bfe_u32 v223, v212, 10, 1
	v_lshl_add_u32 v222, v222, 2, v128
	v_mad_u32_u24 v223, v223, v235, 1
	ds_add_u32 v222, v223
	s_mov_b64 exec, s[64:65]
	v_xor_b32_e32 v213, v196, v189
	v_bfe_u32 v222, v213, 11, 10
	v_bfe_u32 v223, v213, 10, 1
	v_lshl_add_u32 v222, v222, 2, v128
	v_mad_u32_u24 v223, v223, v235, 1
	ds_add_u32 v222, v223
	s_waitcnt lgkmcnt(8)
	s_mov_b64 exec, s[14:15]
	v_or_b32_e32 v104, v105, v104
	ds_bpermute_b32 v105, v145, v104
	s_mov_b64 exec, s[50:51]
	v_cmp_lt_u32_e64 s[66:67], s0, v214
	s_add_i32 s85, s74, 0x0
	v_bfe_u32 v224, v206, 10, 11
	v_lshl_add_u32 v222, v214, 2, v141
	v_add3_u32 v224, v224, v124, s85
	s_andn2_b64 exec, exec, s[66:67]
	ds_write_b32 v222, v224
	s_mov_b64 exec, s[66:67]
	ds_write_b32 v227, v193
	s_mov_b64 exec, s[52:53]
	v_cmp_lt_u32_e64 s[66:67], s0, v215
	s_add_i32 s85, s74, 0x800
	v_bfe_u32 v224, v207, 10, 11
	v_lshl_add_u32 v222, v215, 2, v141
	v_add3_u32 v224, v224, v124, s85
	s_andn2_b64 exec, exec, s[66:67]
	ds_write_b32 v222, v224
	s_mov_b64 exec, s[66:67]
	ds_write_b32 v227, v193
	s_waitcnt lgkmcnt(8)
	s_mov_b64 exec, s[54:55]
	v_cmp_lt_u32_e64 s[66:67], s0, v216
	s_add_i32 s85, s74, 0x1000
	v_bfe_u32 v224, v208, 10, 11
	v_lshl_add_u32 v222, v216, 2, v141
	v_add3_u32 v224, v224, v124, s85
	s_andn2_b64 exec, exec, s[66:67]
	ds_write_b32 v222, v224
	s_mov_b64 exec, s[66:67]
	ds_write_b32 v227, v193
	s_mov_b64 exec, s[56:57]
	v_cmp_lt_u32_e64 s[66:67], s0, v217
	s_add_i32 s85, s74, 0x1800
	v_bfe_u32 v224, v209, 10, 11
	v_lshl_add_u32 v222, v217, 2, v141
	v_add3_u32 v224, v224, v124, s85
	s_andn2_b64 exec, exec, s[66:67]
	ds_write_b32 v222, v224
	s_mov_b64 exec, s[66:67]
	ds_write_b32 v227, v193
	s_waitcnt lgkmcnt(8)
	s_mov_b64 exec, s[58:59]
	v_cmp_lt_u32_e64 s[66:67], s0, v218
	s_add_i32 s85, s74, 0x8000
	v_bfe_u32 v224, v210, 10, 11
	v_lshl_add_u32 v222, v218, 2, v141
	v_add3_u32 v224, v224, v124, s85
	s_andn2_b64 exec, exec, s[66:67]
	ds_write_b32 v222, v224
	s_mov_b64 exec, s[66:67]
	ds_write_b32 v227, v193
	s_mov_b64 exec, s[60:61]
	v_cmp_lt_u32_e64 s[66:67], s0, v219
	s_add_i32 s85, s74, 0x8800
	v_bfe_u32 v224, v211, 10, 11
	v_lshl_add_u32 v222, v219, 2, v141
	v_add3_u32 v224, v224, v124, s85
	s_andn2_b64 exec, exec, s[66:67]
	ds_write_b32 v222, v224
	s_mov_b64 exec, s[66:67]
	ds_write_b32 v227, v193
	s_waitcnt lgkmcnt(8)
	s_mov_b64 exec, s[62:63]
	v_cmp_lt_u32_e64 s[66:67], s0, v220
	s_add_i32 s85, s74, 0x9000
	v_bfe_u32 v224, v212, 10, 11
	v_lshl_add_u32 v222, v220, 2, v141
	v_add3_u32 v224, v224, v124, s85
	s_andn2_b64 exec, exec, s[66:67]
	ds_write_b32 v222, v224
	s_mov_b64 exec, s[66:67]
	ds_write_b32 v227, v193
	s_mov_b64 exec, s[64:65]
	v_cmp_lt_u32_e64 s[66:67], s0, v221
	s_add_i32 s85, s74, 0x9800
	v_bfe_u32 v224, v213, 10, 11
	v_lshl_add_u32 v222, v221, 2, v141
	v_add3_u32 v224, v224, v124, s85
	s_andn2_b64 exec, exec, s[66:67]
	ds_write_b32 v222, v224
	s_mov_b64 exec, s[66:67]
	ds_write_b32 v227, v193
	s_mov_b64 exec, s[14:15]
	s_and_saveexec_b64 s[14:15], s[38:39]
	v_or_b32_e32 v106, v104, v105
	v_lshl_add_u64 v[104:105], v[122:123], 0, s[74:75]
	v_add_co_u32_e32 v104, vcc, 0x3f700000, v104
	s_nop 1
	v_addc_co_u32_e32 v105, vcc, 0, v105, vcc
	global_store_dword v[104:105], v106, off
	s_or_b64 exec, exec, s[14:15]
	s_add_u32 s74, s74, 0x80000
	s_addc_u32 s75, s75, 0
	s_add_i32 s31, s31, 8
	s_cmp_ge_i32 s31, s32
	s_cbranch_scc0 .Lpb2_i0
